# scan A: per-chunk record stores (read one phase later, 200 MB per layer) marked nt
# speedup vs baseline: 1.0014x; 1.0014x over previous
; DI void phase_scan_a(Frame& F, int l, int u_lo, int u_hi, int u_step) {
;     ...
;         { const LAS unsigned char* yb = (wave < 4) ? MB(4) : MB(2); LAS unsigned char* ob = (wave < 4) ? MB(3) : MB(0);
;           const int tm = wave & 3, ysw = (wave < 4) ? 3 : 0;
;           bf16x8 xf[2], yf[4][2]; int lq = lane; asm volatile("" : "+v"(lq));
; #pragma unroll
;           for (int s = 0; s < 2; ++s) { xf[s] = mfrag(MB(11), MP, 16 * tm, s, 0, lq);
; #pragma unroll
;               for (int n = 0; n < 4; ++n) yf[n][s] = mfrag(yb, MP, 16 * n, s, ysw, lq); }
;           PIN8(xf[0]); PIN8(xf[1]);
; #pragma unroll
;           for (int n = 0; n < 4; ++n) { PIN8(yf[n][0]); PIN8(yf[n][1]); }
; #pragma unroll
;           for (int tn = 0; tn < 4; ++tn) { f32x4 acc = {0.f, 0.f, 0.f, 0.f};
;               acc = mfma16(xf[0], yf[tn][0], acc); acc = mfma16(xf[1], yf[tn][1], acc);
;               *(LAS u32x2*)(ob + (16 * tn + r16) * MP + (16 * tm + 4 * g) * 2) = pk4(acc); } }
;         __syncthreads();
;         }
;     ...
;         asm volatile("" : "+v"(plw[0]), "+v"(plw[1]), "+v"(plw[2]), "+v"(plw[3]), "+v"(plw[4]), "+v"(plw[5]), "+v"(plw[6]), "+v"(plw[7]), "+v"(prv), "+v"(pkv), "+v"(pav), "+v"(pbv), "+v"(pvv));
;     ...
;         SA_REP(16) {
;         { const int tm = wave >> 1;
;           bf16x8 x3[2], x0[2], x6[2], y9[2][2], y6[2][2], y0[2][2]; u32x2 rrv[2]; int lq = lane; asm volatile("" : "+v"(lq));
; #pragma unroll
;           for (int s = 0; s < 2; ++s) { x3[s] = mfrag(MB(3), MP, 16 * tm, s, 0, lq); x0[s] = mfrag(MB(0), MP, 16 * tm, s, 0, lq); x6[s] = mfrag(MB(6), MP, 16 * tm, s, 3, lq);
; #pragma unroll
;               for (int q = 0; q < 2; ++q) { const int tn = (wave * 2 + q) & 3; y9[q][s] = mfrag(MB(9), MP, 16 * tn, s, 0, lq); y6[q][s] = mfrag(MB(6), MP, 16 * tn, s, 3, lq); y0[q][s] = mfrag(MB(0), MP, 16 * tn, s, 0, lq); } }
; #pragma unroll
;           for (int q = 0; q < 2; ++q) { const int tn = (wave * 2 + q) & 3; rrv[q] = *(const LAS u32x2*)(MB(1) + (16 * tn + r16) * MP + (16 * tm + 4 * g) * 2); }
;           PIN8(x3[0]); PIN8(x3[1]); PIN8(x0[0]); PIN8(x0[1]); PIN8(x6[0]); PIN8(x6[1]);
; #pragma unroll
;           for (int q = 0; q < 2; ++q) { PIN8(y9[q][0]); PIN8(y9[q][1]); PIN8(y6[q][0]); PIN8(y6[q][1]); PIN8(y0[q][0]); PIN8(y0[q][1]); PIN8(rrv[q]); }
; #pragma unroll
;           for (int q = 0; q < 2; ++q) { const int tn = (wave * 2 + q) & 3;
.LBB0_1140:
	v_mov_b32_e32 v36, v210
	s_waitcnt lgkmcnt(0)
	s_barrier
	v_readlane_b32 s42, v255, 41
	v_and_b32_e32 v37, 15, v36
	s_movk_i32 s60, 0x90
	v_or_b32_e32 v39, s42, v37
	v_readlane_b32 s42, v255, 11
	v_lshrrev_b32_e32 v38, 4, v36
	v_and_b32_e32 v36, -16, v36
	v_mov_b32_e32 v40, s42
	v_readlane_b32 s42, v255, 40
	v_mad_u32_u24 v39, v39, s60, v40
	v_readlane_b32 s43, v254, 5
	v_mov_b32_e32 v40, s42
	v_mad_u32_u24 v37, v37, s60, v40
	v_readlane_b32 s42, v254, 4
	v_add_u32_e32 v40, v39, v36
	v_add_u32_e32 v41, v37, v36
	v_xor_b32_e32 v36, s42, v38
	v_lshl_add_u32 v52, v36, 4, v37
	v_xor_b32_e32 v36, s43, v38
	v_readlane_b32 s56, v254, 6
	v_lshl_add_u32 v56, v36, 4, v37
	s_ashr_i32 s40, s62, 5
	v_xor_b32_e32 v36, s56, v38
	v_lshl_add_u32 v66, v36, 4, v37
	v_add_u32_e32 v36, 4, v38
	v_lshlrev_b32_e32 v38, 4, v36
	v_add_u32_e32 v60, v39, v38
	v_add_u32_e32 v44, v37, v38
	v_xor_b32_e32 v38, s42, v36
	v_lshl_add_u32 v48, v38, 4, v37
	v_xor_b32_e32 v38, s43, v36
	v_xor_b32_e32 v36, s56, v36
	v_lshl_add_u32 v70, v38, 4, v37
	v_lshl_add_u32 v74, v36, 4, v37
	ds_read_b128 v[36:39], v40
	ds_read_b128 v[40:43], v41
	ds_read_b128 v[44:47], v44
	ds_read_b128 v[48:51], v48 offset:2304
	ds_read_b128 v[52:55], v52 offset:2304
	ds_read_b128 v[56:59], v56 offset:4608
	ds_read_b128 v[60:63], v60
	ds_read_b128 v[66:69], v66 offset:6912
	ds_read_b128 v[70:73], v70 offset:4608
	ds_read_b128 v[74:77], v74 offset:6912
	s_waitcnt lgkmcnt(9)
	s_waitcnt lgkmcnt(3)
	s_waitcnt lgkmcnt(1)
	v_mfma_f32_16x16x32_bf16 v[40:43], v[36:39], v[40:43], 0
	s_waitcnt lgkmcnt(0)
	s_and_b32 s41, s66, 0xf80
	v_mfma_f32_16x16x32_bf16 v[40:43], v[60:63], v[44:47], v[40:43]
	s_add_i32 s40, s41, s40
	s_ashr_i32 s41, s40, 31
	s_lshl_b64 s[58:59], s[40:41], 14
	v_mfma_f32_16x16x32_bf16 v[44:47], v[36:39], v[52:55], 0
	v_readlane_b32 s40, v255, 17
	s_nop 2
	v_cvt_pk_bf16_f32 v40, v40, v41
	v_cvt_pk_bf16_f32 v41, v42, v43
	v_mfma_f32_16x16x32_bf16 v[44:47], v[60:63], v[48:51], v[44:47]
	ds_write_b64 v207, v[40:41]
	s_add_u32 s42, s40, s58
	v_readlane_b32 s40, v255, 18
	v_mfma_f32_16x16x32_bf16 v[48:51], v[36:39], v[56:59], 0
	s_addc_u32 s43, s40, s59
	s_nop 2
	v_cvt_pk_bf16_f32 v44, v44, v45
	v_cvt_pk_bf16_f32 v45, v46, v47
	v_mfma_f32_16x16x32_bf16 v[36:39], v[36:39], v[66:69], 0
	ds_write_b64 v207, v[44:45] offset:2304
	v_readlane_b32 s40, v255, 33
	v_readlane_b32 s41, v255, 13
	v_mfma_f32_16x16x32_bf16 v[36:39], v[60:63], v[74:77], v[36:39]
	v_readlane_b32 vcc_lo, v254, 7
	s_mov_b32 s70, s61
	v_mov_b32_e32 v45, s69
	v_mfma_f32_16x16x32_bf16 v[40:43], v[60:63], v[70:73], v[48:51]
	s_add_u32 s56, s42, 0x2000
	s_nop 2
	v_cvt_pk_bf16_f32 v36, v36, v37
	v_cvt_pk_bf16_f32 v37, v38, v39
	ds_write_b64 v207, v[36:37] offset:6912
	v_mov_b32_e32 v36, v210
	v_cvt_pk_bf16_f32 v40, v40, v41
	v_cvt_pk_bf16_f32 v41, v42, v43
	ds_write_b64 v207, v[40:41] offset:4608
	s_waitcnt lgkmcnt(0)
	s_barrier
	s_waitcnt vmcnt(0)
	s_addc_u32 s57, s43, 0
	v_and_b32_e32 v37, 15, v36
	v_or_b32_e32 v39, s40, v37
	v_mul_lo_u32 v39, v39, s60
	s_mov_b32 s40, s69
	v_lshrrev_b32_e32 v38, 4, v36
	v_add_u32_e32 v39, s40, v39
	v_and_b32_e32 v36, -16, v36
	v_or_b32_e32 v40, s61, v37
	v_add_u32_e32 v41, v39, v36
	v_add_u32_e32 v43, s41, v36
	v_add_u32_e32 v36, s40, v36
	v_or_b32_e32 v37, vcc_lo, v37
	v_readlane_b32 s61, v255, 42
	v_mad_u32_u24 v48, v40, s60, v36
	v_mad_u32_u24 v50, v37, s60, v36
	v_add_u32_e32 v36, 4, v38
	v_xor_b32_e32 v42, s61, v38
	v_mad_u32_u24 v44, v40, s60, v43
	v_mad_u32_u24 v46, v40, s60, v45
	v_xor_b32_e32 v47, s33, v38
	v_mad_u32_u24 v49, v37, s60, v43
	v_mad_u32_u24 v43, v37, s60, v45
	v_xor_b32_e32 v45, s44, v38
	v_lshlrev_b32_e32 v38, 4, v36
	v_xor_b32_e32 v52, s61, v36
	v_lshl_add_u32 v42, v42, 4, v39
	v_add_u32_e32 v51, v39, v38
	v_lshl_add_u32 v39, v52, 4, v39
	v_add_u32_e32 v52, s41, v38
	v_add_u32_e32 v38, s40, v38
	v_xor_b32_e32 v53, s33, v36
	v_xor_b32_e32 v36, s44, v36
	v_lshl_add_u32 v47, v47, 4, v46
	v_lshl_add_u32 v45, v45, 4, v43
	v_mad_u32_u24 v56, v40, s60, v52
	v_lshl_add_u32 v46, v53, 4, v46
	v_mad_u32_u24 v57, v40, s60, v38
	v_mad_u32_u24 v58, v37, s60, v52
	v_lshl_add_u32 v78, v36, 4, v43
	v_mad_u32_u24 v225, v37, s60, v38
	ds_read_b64 v[222:223], v208 offset:9216
	ds_read_b64 v[126:127], v209 offset:9216
	ds_read_b128 v[74:77], v41 offset:27648
	ds_read_b128 v[52:55], v41
	ds_read_b128 v[70:73], v51 offset:27648
	ds_read_b128 v[36:39], v39 offset:55296
	ds_read_b128 v[40:43], v42 offset:55296
	ds_read_b128 v[98:101], v44
	ds_read_b128 v[94:97], v56
	ds_read_b128 v[102:105], v46 offset:55296
	ds_read_b128 v[202:205], v47 offset:55296
	ds_read_b128 v[86:89], v48
	ds_read_b128 v[90:93], v57
	ds_read_b128 v[56:59], v58
	ds_read_b128 v[60:63], v49
	ds_read_b128 v[82:85], v45 offset:55296
	ds_read_b128 v[66:69], v51
	ds_read_b128 v[44:47], v50
	ds_read_b128 v[78:81], v78 offset:55296
	ds_read_b128 v[48:51], v225
	s_waitcnt lgkmcnt(14)
	s_waitcnt lgkmcnt(3)
	s_nop 0
	v_mfma_f32_16x16x32_bf16 v[226:229], v[74:77], v[98:101], 0
	v_mfma_f32_16x16x32_bf16 v[202:205], v[74:77], v[202:205], 0
	v_lshlrev_b32_e32 v234, 16, v222
	v_and_b32_e32 v235, 0xffff0000, v222
	v_lshlrev_b32_e32 v222, 16, v223
	v_mfma_f32_16x16x32_bf16 v[226:229], v[70:73], v[94:97], v[226:229]
	v_and_b32_e32 v223, 0xffff0000, v223
	s_waitcnt lgkmcnt(1)
	v_mfma_f32_16x16x32_bf16 v[102:105], v[70:73], v[102:105], v[202:205]
	s_nop 4
	v_add_f32_e64 v226, v226, v234
	v_add_f32_e64 v227, v227, v235
	v_pk_add_f32 v[222:223], v[228:229], v[222:223]
	v_cvt_pk_bf16_f32 v226, v226, v227
	v_cvt_pk_bf16_f32 v227, v222, v223
	v_lshl_add_u64 v[222:223], s[56:57], 0, v[114:115]
	s_waitcnt lgkmcnt(0)
	global_store_dwordx2 v[222:223], v[226:227], off nt
	s_or_b64 s[40:41], s[92:93], s[94:95]
	s_or_b64 s[40:41], s[40:41], s[96:97]
	s_or_b64 s[40:41], s[40:41], s[4:5]
	s_and_b64 s[40:41], s[40:41], exec
	s_cbranch_scc0 .Lsa8_g1_done
	ds_read_b32 v202, v184
	s_mov_b64 s[40:41], exec
	s_waitcnt lgkmcnt(0)
	s_and_b64 exec, s[40:41], s[92:93]
	v_add_f32_e32 v102, v102, v202
	s_and_b64 exec, s[40:41], s[94:95]
	v_add_f32_e32 v103, v103, v202
	s_and_b64 exec, s[40:41], s[96:97]
	v_add_f32_e32 v104, v104, v202
	s_and_b64 exec, s[40:41], s[4:5]
	v_add_f32_e32 v105, v105, v202
	s_mov_b64 exec, s[40:41]

; DI float bflo(unsigned w) { return __uint_as_float(w << 16); }
; DI float bfhi(unsigned w) { return __uint_as_float(w & 0xffff0000u); }
; DI f32x4 mfma16(bf16x8 a, bf16x8 b, f32x4 c) { return __builtin_amdgcn_mfma_f32_16x16x32_bf16(a, b, c, 0, 0, 0); }
; DI int permk(int k) { return (k & 32) | (((k >> 2) & 3) << 3) | (((k >> 4) & 1) << 2) | (k & 3); }
; DI u32x2 pk4(f32x4 v) { u32x2 w; w.x = pk2(v[0], v[1]); w.y = pk2(v[2], v[3]); return w; }
; DI void phase_scan_a(Frame& F, int l, int u_lo, int u_hi, int u_step) {
;     ...
;           for (int q = 0; q < 2; ++q) { const int tn = (wave * 2 + q) & 3;
;             { f32x4 acc = {0.f, 0.f, 0.f, 0.f}; acc = mfma16(x3[0], y9[q][0], acc); acc = mfma16(x3[1], y9[q][1], acc);
;               const int i = 16 * tn + r16, k0 = 16 * tm + 4 * g; const u32x2 rr = rrv[q];
;               acc[0] += bflo(rr.x); acc[1] += bfhi(rr.x); acc[2] += bflo(rr.y); acc[3] += bfhi(rr.y);
;               *(u32x2*)(rec1 + U_RPP + (size_t)(i * 64 + permk(k0)) * 2) = pk4(acc); }
;             { f32x4 acc = {0.f, 0.f, 0.f, 0.f}; acc = mfma16(x3[0], y6[q][0], acc); acc = mfma16(x3[1], y6[q][1], acc);
;               const int kp = 16 * tn + r16, k0 = 16 * tm + 4 * g;
; #pragma unroll
;               for (int r = 0; r < 4; ++r) if (k0 + r == kp) acc[r] += GL[kp];
;               *(u32x2*)(rec1 + U_PMP + (size_t)(kp * 64 + permk(k0)) * 2) = pk4(acc); }
;             { f32x4 acc = pyl[q]; acc = mfma16(x0[0], y9[q][0], acc); acc = mfma16(x0[1], y9[q][1], acc); if (wave == 0) acc = mm_tile(MB(5), MP, 16 * tm, MB(10), MP, 16 * tn, 2, acc, lane, 3, 0);
;               *(u32x2*)(rec2 + U_YLT + (size_t)((16 * tn + r16) * 64 + 16 * tm + 4 * g) * 2) = pk4(acc); }
;             { f32x4 acc = pqm[q]; acc = mfma16(x6[0], y0[q][0], acc); acc = mfma16(x6[1], y0[q][1], acc); if (wave == 0) acc = mm_tile(MB(7), MP, 16 * tm, MB(5), MP, 16 * tn, 2, acc, lane, 3, 3);
;               *(u32x2*)(rec2 + U_QMT + (size_t)((16 * tn + r16) * 64 + 16 * tm + 4 * g) * 2) = pk4(acc); }
.Lsa8_g1_join:
	v_mfma_f32_16x16x32_bf16 v[32:35], v[52:55], v[98:101], v[32:35]
	v_readlane_b32 s60, v255, 26
	v_readlane_b32 s61, v255, 27
	v_cvt_pk_bf16_f32 v102, v102, v103
	v_mfma_f32_16x16x32_bf16 v[32:35], v[66:69], v[94:97], v[32:35]
	v_cndmask_b32_e64 v98, 0, 1, s[60:61]
	v_cvt_pk_bf16_f32 v103, v104, v105
	v_lshl_add_u64 v[104:105], s[42:43], 0, v[114:115]
	v_cmp_ne_u32_e64 s[40:41], 1, v98
	s_andn2_b64 vcc, exec, s[60:61]
	global_store_dwordx2 v[104:105], v[102:103], off nt
	s_cbranch_vccnz .LBB0_1154
	ds_read_b128 v[94:97], v221 offset:46080
	ds_read_b128 v[98:101], v216
	ds_read_b128 v[236:239], v221 offset:46144
	ds_read_b128 v[240:243], v216 offset:64
	s_waitcnt lgkmcnt(2)
	v_mfma_f32_16x16x32_bf16 v[32:35], v[94:97], v[98:101], v[32:35]
	s_waitcnt lgkmcnt(0)
	v_mfma_f32_16x16x32_bf16 v[32:35], v[236:239], v[240:243], v[32:35]
.LBB0_1154:
	v_mfma_f32_16x16x32_bf16 v[28:31], v[40:43], v[86:89], v[28:31]
	v_readlane_b32 s60, v255, 15
	s_add_u32 s58, s60, s58
	v_readlane_b32 s60, v255, 16
	s_addc_u32 s59, s60, s59
	v_mfma_f32_16x16x32_bf16 v[28:31], v[36:39], v[90:93], v[28:31]
	s_add_u32 s60, s58, 0x2000
	s_addc_u32 s61, s59, 0
	v_cvt_pk_bf16_f32 v32, v32, v33
	v_cvt_pk_bf16_f32 v33, v34, v35
	v_lshl_add_u64 v[34:35], s[60:61], 0, v[116:117]
	s_and_b64 vcc, exec, s[40:41]
	global_store_dwordx2 v[34:35], v[32:33], off nt
	s_cbranch_vccnz .LBB0_1156
	ds_read_b128 v[32:35], v221 offset:64512
	ds_read_b128 v[86:89], v217 offset:46080
	ds_read_b128 v[236:239], v221 offset:64576
	ds_read_b128 v[240:243], v217 offset:46144
	s_waitcnt lgkmcnt(2)
	v_mfma_f32_16x16x32_bf16 v[28:31], v[32:35], v[86:89], v[28:31]
	s_waitcnt lgkmcnt(0)
	v_mfma_f32_16x16x32_bf16 v[28:31], v[236:239], v[240:243], v[28:31]
.LBB0_1156:
	s_nop 7
	v_cvt_pk_bf16_f32 v28, v28, v29
	v_cvt_pk_bf16_f32 v29, v30, v31
	v_lshl_add_u64 v[30:31], s[58:59], 0, v[116:117]
	global_store_dwordx2 v[30:31], v[28:29], off nt
	v_mfma_f32_16x16x32_bf16 v[28:31], v[74:77], v[60:63], 0
	v_lshlrev_b32_e32 v32, 16, v126
	v_and_b32_e32 v33, 0xffff0000, v126
	v_mfma_f32_16x16x32_bf16 v[28:31], v[70:73], v[56:59], v[28:31]
	s_nop 7
	v_pk_add_f32 v[28:29], v[28:29], v[32:33]
	v_lshlrev_b32_e32 v32, 16, v127
	v_and_b32_e32 v33, 0xffff0000, v127
	v_pk_add_f32 v[30:31], v[30:31], v[32:33]
	v_cvt_pk_bf16_f32 v28, v28, v29
	v_cvt_pk_bf16_f32 v29, v30, v31
	v_lshl_add_u64 v[30:31], s[56:57], 0, v[118:119]
	global_store_dwordx2 v[30:31], v[28:29], off nt
	v_mfma_f32_16x16x32_bf16 v[28:31], v[74:77], v[82:85], 0
	v_mfma_f32_16x16x32_bf16 v[28:31], v[70:73], v[78:81], v[28:31]
	s_or_b64 s[56:57], s[6:7], s[10:11]
	s_or_b64 s[56:57], s[56:57], s[2:3]
	s_or_b64 s[56:57], s[56:57], s[0:1]
	s_and_b64 s[56:57], s[56:57], exec
	s_cbranch_scc0 .Lsa8_g2_done
	ds_read_b32 v32, v185
	s_mov_b64 s[56:57], exec
	s_waitcnt lgkmcnt(0)
	s_and_b64 exec, s[56:57], s[6:7]
	v_add_f32_e32 v28, v28, v32
	s_and_b64 exec, s[56:57], s[10:11]
	v_add_f32_e32 v29, v29, v32
	s_and_b64 exec, s[56:57], s[2:3]
	v_add_f32_e32 v30, v30, v32
	s_and_b64 exec, s[56:57], s[0:1]
	v_add_f32_e32 v31, v31, v32
	s_mov_b64 exec, s[56:57]
.Lsa8_g2_done:
	s_nop 3
	v_mfma_f32_16x16x32_bf16 v[24:27], v[52:55], v[60:63], v[24:27]
	v_cvt_pk_bf16_f32 v28, v28, v29
	v_cvt_pk_bf16_f32 v29, v30, v31
	v_lshl_add_u64 v[30:31], s[42:43], 0, v[118:119]
	v_mfma_f32_16x16x32_bf16 v[24:27], v[66:69], v[56:59], v[24:27]
	s_and_b64 vcc, exec, s[40:41]
	global_store_dwordx2 v[30:31], v[28:29], off nt
	s_cbranch_vccnz .LBB0_1166
	ds_read_b128 v[28:31], v221 offset:46080
	ds_read_b128 v[32:35], v218
	ds_read_b128 v[236:239], v221 offset:46144
	ds_read_b128 v[240:243], v218 offset:64
	s_waitcnt lgkmcnt(2)
	v_mfma_f32_16x16x32_bf16 v[24:27], v[28:31], v[32:35], v[24:27]
	s_waitcnt lgkmcnt(0)
	v_mfma_f32_16x16x32_bf16 v[24:27], v[236:239], v[240:243], v[24:27]
.LBB0_1166:
	v_mfma_f32_16x16x32_bf16 v[20:23], v[40:43], v[44:47], v[20:23]
	s_nop 6
	v_cvt_pk_bf16_f32 v24, v24, v25
	v_cvt_pk_bf16_f32 v25, v26, v27
	v_lshl_add_u64 v[26:27], s[60:61], 0, v[120:121]
	v_mfma_f32_16x16x32_bf16 v[20:23], v[36:39], v[48:51], v[20:23]
	s_and_b64 vcc, exec, s[40:41]
	global_store_dwordx2 v[26:27], v[24:25], off nt
	s_cbranch_vccnz .LBB0_1013
	ds_read_b128 v[24:27], v221 offset:64512
	ds_read_b128 v[28:31], v219 offset:46080
	ds_read_b128 v[236:239], v221 offset:64576
	ds_read_b128 v[240:243], v220 offset:46080
	s_waitcnt lgkmcnt(2)
	v_mfma_f32_16x16x32_bf16 v[20:23], v[24:27], v[28:31], v[20:23]
	s_waitcnt lgkmcnt(0)
	v_mfma_f32_16x16x32_bf16 v[20:23], v[236:239], v[240:243], v[20:23]
	s_branch .LBB0_1013
